# read wide: mixer A bias fragments by ds_read_b64 from a parity-split second table copy in 15.5 KiB of newly declared static LDS (was 8 ds_read2_b32 per tile)
# baseline (speedup 1.0000x reference)
; __device__ __forceinline__ void mixer_a_phase(const bf16* AQ, const bf16* AK, const bf16* AV  , bf16* O, float* ST, float* ML, const float* rel_bias, LAS unsigned char* lds, int G, int blk, int tid, int lane, int wave) {
;     ...
;             for (int idx = tid; idx < 3 * TA_LEN; idx += NWAVES * 64) { const int br = idx / TA_LEN, i = idx % TA_LEN - TA_OFF, dil = br == 0 ? 1 : (br == 1 ? 4 : 16);
;                 tab[idx] = (i >= 0 && i <= 128) ? (rel_bias[h * 32 + t5_bucket((i - 64) * dil)] * LOG2E + 64.0f) * KAPPA : -1.0f; }
.LBB0_350:
	s_or_b64 exec, exec, s[22:23]
	s_movk_i32 s1, 0xcff
	v_add_u32_e32 v11, 0x2427c, v4
	ds_write_b32 v4, v2
	ds_write_b32 v11, v2
	v_add_u32_e32 v2, 0x200, v5
	v_cmp_lt_i32_e32 vcc, s1, v5
	v_add_u32_e32 v4, 0x800, v4
	s_or_b64 s[10:11], vcc, s[10:11]
	v_mov_b32_e32 v5, v2
	s_andn2_b64 exec, exec, s[10:11]
	s_cbranch_execz .LBB0_356

; #define LAS __attribute__((address_space(3)))
; #define BA_LOAD(kn, vn, kt_) do { const int kb_ = kb_first + 32 * (kt_); \
;         _Pragma("unroll") for (int ii = 0; ii < 4; ++ii) { const size_t row_ = (size_t)(res + dil * (kb_ + vr + 8 * ii)); \
;             kn[ii] = *(const v4u*)(Kb + row_ * kpitch + 8 * vc); vn[ii] = *(const v4u*)(Vb + row_ * vpitch + 8 * vc); } } while (0)
; #define BA_TR(off_) __builtin_bit_cast(s16x4, __builtin_amdgcn_ds_read_tr16_b64_v4i16((LAS v4i16_t*)(trb + (off_))))
; #define BA_LOAD(kn, vn, kt_) do { const int kb_ = kb_first + 32 * (kt_); \
;         _Pragma("unroll") for (int ii = 0; ii < 4; ++ii) { const size_t row_ = (size_t)(res + dil * (kb_ + vr + 8 * ii)); \
;             kn[ii] = *(const v4u*)(Kb + row_ * kpitch + 8 * vc); vn[ii] = *(const v4u*)(Vb + row_ * vpitch + 8 * vc); } } while (0)
; #define BA_TR(off_) __builtin_bit_cast(s16x4, __builtin_amdgcn_ds_read_tr16_b64_v4i16((LAS v4i16_t*)(trb + (off_))))
; #define BA_TR(off_) __builtin_bit_cast(s16x4, __builtin_amdgcn_ds_read_tr16_b64_v4i16((LAS v4i16_t*)(trb + (off_))))
; #define BA_TR(off_) __builtin_bit_cast(s16x4, __builtin_amdgcn_ds_read_tr16_b64_v4i16((LAS v4i16_t*)(trb + (off_))))
; __device__ __forceinline__ void band_branch_fast(f32x16& o0, f32x16& o1, f32x4& lsum, unsigned& orw, const bf16x8 (&qf)[4], ...
;     ...
;     if (kt_lo < kt_hi) BA_LOAD(kn, vn, kt_lo);
;     for (int kt = kt_lo; kt < kt_hi; ++kt) {
; #pragma unroll
;         for (int ii = 0; ii < 4; ++ii) { const int r_ = vr + 8 * ii; *(LAS v4u*)(kst + r_ * 128 + ((vc ^ (r_ & 7)) * 16)) = kn[ii]; *(LAS v4u*)(vst + r_ * 128 + vc * 16) = vn[ii]; }
;         if (kt + 1 < kt_hi) BA_LOAD(kn, vn, kt + 1);
;         bf16x8 kf[4];
; #pragma unroll
;         for (int d0 = 0; d0 < 4; ++d0) kf[d0] = *(const LAS bf16x8*)(krd + (((2 * d0 + hh) ^ (pi & 7)) * 16));
;         const LAS float* tp = tab + (kb_first + 32 * kt + tboff);
;         f32x16 s;
; #pragma unroll
;         for (int r = 0; r < 16; ++r) s[r] = tp[(r & 7) + 16 * (r >> 3)];
;         s16x4 vt[8];
; #pragma unroll
;         for (int i = 0; i < 8; ++i) vt[i] = BA_TR((i >> 2) * 2048 + ((i >> 1) & 1) * 64 + (i & 1) * 512);
;         __builtin_amdgcn_sched_barrier(0);
; #pragma unroll
;         for (int d0 = 0; d0 < 4; ++d0) s = __builtin_amdgcn_mfma_f32_32x32x16_bf16(kf[d0], qf[d0], s, 0, 0, 0);
.Lmx1_p1:
	v_mov_b32_e32 v20, 0
	v_lshl_add_u32 v69, s15, 7, v206
	v_and_b32_e32 v36, 4, v69
	v_mul_u32_u24_e32 v36, 0x909f, v36
	v_add_u32_e32 v69, v69, v36
	v_mov_b32_e32 v127, 0
	v_mov_b32_e32 v126, v162
	s_mov_b32 s46, s15
	v_mov_b32_e32 v21, v20
	v_mov_b32_e32 v22, v20
	v_mov_b32_e32 v23, v20
	v_mov_b32_e32 v24, v20
	v_mov_b32_e32 v25, v20
	v_mov_b32_e32 v26, v20
	v_mov_b32_e32 v27, v20
	v_mov_b32_e32 v28, v20
	v_mov_b32_e32 v29, v20
	v_mov_b32_e32 v30, v20
	v_mov_b32_e32 v31, v20
	v_mov_b32_e32 v32, v20
	v_mov_b32_e32 v33, v20
	v_mov_b32_e32 v34, v20
	v_mov_b32_e32 v35, v20
	v_mov_b32_e32 v4, v20
	v_mov_b32_e32 v5, v20
	v_mov_b32_e32 v6, v20
	v_mov_b32_e32 v7, v20
	v_mov_b32_e32 v8, v20
	v_mov_b32_e32 v9, v20
	v_mov_b32_e32 v10, v20
	v_mov_b32_e32 v11, v20
	v_mov_b32_e32 v12, v20
	v_mov_b32_e32 v13, v20
	v_mov_b32_e32 v14, v20
	v_mov_b32_e32 v15, v20
	v_mov_b32_e32 v16, v20
	v_mov_b32_e32 v17, v20
	v_mov_b32_e32 v18, v20
	v_mov_b32_e32 v19, v20
	v_mov_b32_e32 v90, v20
	v_mov_b32_e32 v91, v20
	v_mov_b32_e32 v92, v20
	v_mov_b32_e32 v93, v20
	s_branch .LBB0_362
.LBB0_361:
	v_add3_u32 v36, v195, v200, s99
	v_add3_u32 v37, v195, v201, s99
	ds_read_b128 v[128:131], v36 offset:20480
	ds_read_b128 v[132:135], v37 offset:20480
	v_add3_u32 v36, v195, v202, s99
	v_add3_u32 v37, v195, v203, s99
	ds_read_b128 v[164:167], v36 offset:20480
	ds_read_b128 v[168:171], v37 offset:20480
	ds_read_b64 v[36:37], v69
	ds_read_b64 v[38:39], v69 offset:8
	ds_read_b64 v[40:41], v69 offset:16
	ds_read_b64 v[42:43], v69 offset:24
	ds_read_b64 v[44:45], v69 offset:64
	ds_read_b64 v[46:47], v69 offset:72
	ds_read_b64 v[48:49], v69 offset:80
	ds_read_b64 v[50:51], v69 offset:88
	v_add3_u32 v136, v194, v193, s99
	ds_read_b64_tr_b16 v[172:173], v136 offset:16384
	ds_read_b64_tr_b16 v[174:175], v136 offset:16896
	ds_read_b64_tr_b16 v[178:179], v136 offset:16960
	ds_read_b64_tr_b16 v[176:177], v136 offset:16448
	ds_read_b64_tr_b16 v[180:181], v136 offset:18432
	ds_read_b64_tr_b16 v[182:183], v136 offset:18944
	ds_read_b64_tr_b16 v[186:187], v136 offset:19008
	ds_read_b64_tr_b16 v[184:185], v136 offset:18496
	s_waitcnt lgkmcnt(8)
	v_mfma_f32_32x32x16_bf16 v[36:51], v[128:131], v[52:55], v[36:51]
	v_mfma_f32_32x32x16_bf16 v[36:51], v[132:135], v[56:59], v[36:51]
	v_mfma_f32_32x32x16_bf16 v[36:51], v[164:167], v[60:63], v[36:51]
	v_mfma_f32_32x32x16_bf16 v[36:51], v[168:171], v[64:67], v[36:51]
	s_waitcnt lgkmcnt(0)
	s_add_i32 s46, s46, 1
	s_cmp_lt_i32 s46, s16
	s_cbranch_scc0 .Lmx1_skip
	s_add_i32 m0, s98, 0x1000
	s_nop 0
	global_load_lds_dwordx4 v[94:95], off
	s_add_i32 m0, s98, 0x0
	v_lshl_add_u64 v[94:95], v[94:95], 0, s[100:101]
	global_load_lds_dwordx4 v[96:97], off
	s_add_i32 m0, s98, 0x1400
	v_lshl_add_u64 v[96:97], v[96:97], 0, s[100:101]
	global_load_lds_dwordx4 v[98:99], off
	s_add_i32 m0, s98, 0x400
	v_lshl_add_u64 v[98:99], v[98:99], 0, s[100:101]
	global_load_lds_dwordx4 v[100:101], off
	s_add_i32 m0, s98, 0x1800
	v_lshl_add_u64 v[100:101], v[100:101], 0, s[100:101]
	global_load_lds_dwordx4 v[102:103], off
	s_add_i32 m0, s98, 0x800
	v_lshl_add_u64 v[102:103], v[102:103], 0, s[100:101]
	global_load_lds_dwordx4 v[104:105], off
	s_add_i32 m0, s98, 0x1c00
	v_lshl_add_u64 v[104:105], v[104:105], 0, s[100:101]
	global_load_lds_dwordx4 v[106:107], off
	s_add_i32 m0, s98, 0xc00
	v_lshl_add_u64 v[106:107], v[106:107], 0, s[100:101]
	global_load_lds_dwordx4 v[108:109], off
	v_lshl_add_u64 v[108:109], v[108:109], 0, s[100:101]

; #define LAS __attribute__((address_space(3)))
; #define BA_TR(off_) __builtin_bit_cast(s16x4, __builtin_amdgcn_ds_read_tr16_b64_v4i16((LAS v4i16_t*)(trb + (off_))))
; #define BA_TR(off_) __builtin_bit_cast(s16x4, __builtin_amdgcn_ds_read_tr16_b64_v4i16((LAS v4i16_t*)(trb + (off_))))
; #define BA_TR(off_) __builtin_bit_cast(s16x4, __builtin_amdgcn_ds_read_tr16_b64_v4i16((LAS v4i16_t*)(trb + (off_))))
; #define BA_TR(off_) __builtin_bit_cast(s16x4, __builtin_amdgcn_ds_read_tr16_b64_v4i16((LAS v4i16_t*)(trb + (off_))))
; __device__ __forceinline__ void band_branch_fast(f32x16& o0, f32x16& o1, f32x4& lsum, unsigned& orw, const bf16x8 (&qf)[4], ...
;     ...
;         const LAS float* tp = tab + (kb_first + 32 * kt + tboff);
;         f32x16 s;
; #pragma unroll
;         for (int r = 0; r < 16; ++r) s[r] = tp[(r & 7) + 16 * (r >> 3)];
;         s16x4 vt[8];
; #pragma unroll
;         for (int i = 0; i < 8; ++i) vt[i] = BA_TR((i >> 2) * 2048 + ((i >> 1) & 1) * 64 + (i & 1) * 512);
;         __builtin_amdgcn_sched_barrier(0);
; #pragma unroll
;         for (int d0 = 0; d0 < 4; ++d0) s = __builtin_amdgcn_mfma_f32_32x32x16_bf16(kf[d0], qf[d0], s, 0, 0, 0);
; __device__ __forceinline__ void mixer_a_phase(const bf16* AQ, const bf16* AK, const bf16* AV  , bf16* O, float* ST, float* ML, const float* rel_bias, LAS unsigned char* lds, int G, int blk, int tid, int lane, int wave) {
;     ...
;             if (__builtin_expect(!exact, 1)) {
;                 f32x4 lsum = {0.f, 0.f, 0.f, 0.f}; unsigned orw = 0u;
;                 band_branch_fast(o0, o1, lsum, orw, qf, Kb, 512, Vb, 512, 16, r, 512, 32 * (a - 2), 5, tab + 2 * TA_LEN, -(32 * a + i5) + 64 + TA_OFF + 8 * hh, vst, lane);
;                 band_branch_fast(o0, o1, lsum, orw, qf, Kb, 512, Vb, 512, 4, r & 3, 2048, 128 * a - 64, 8, tab + TA_LEN, -(128 * a + 4 * i5 + (r >> 2)) + 64 + TA_OFF + 8 * hh, vst, lane);
.LBB0_390:
	s_andn2_b64 vcc, exec, s[10:11]
	s_cbranch_vccnz .LBB0_395
	v_mov_b32_e32 v54, 0
	v_mov_b32_e32 v136, 0
	v_mov_b32_e32 v4, v224
	v_mov_b32_e32 v2, v223
	v_and_b32_e32 v5, 4, v2
	v_mul_u32_u24_e32 v5, 0x909f, v5
	v_add_u32_e32 v2, v2, v5
	s_mov_b32 s0, s34
	v_mov_b32_e32 v55, v54
	v_mov_b32_e32 v56, v54
	v_mov_b32_e32 v57, v54
	s_branch .LBB0_393
.LBB0_392:
	v_add3_u32 v5, v195, v200, s99
	v_add3_u32 v38, v195, v201, s99
	ds_read_b128 v[130:133], v5 offset:20480
	ds_read_b128 v[186:189], v38 offset:20480
	v_add3_u32 v5, v195, v202, s99
	v_add3_u32 v38, v195, v203, s99
	ds_read_b128 v[226:229], v5 offset:20480
	ds_read_b128 v[230:233], v38 offset:20480
	ds_read_b64 v[38:39], v2
	ds_read_b64 v[40:41], v2 offset:8
	ds_read_b64 v[42:43], v2 offset:16
	ds_read_b64 v[44:45], v2 offset:24
	ds_read_b64 v[46:47], v2 offset:64
	ds_read_b64 v[48:49], v2 offset:72
	ds_read_b64 v[50:51], v2 offset:80
	ds_read_b64 v[52:53], v2 offset:88
	v_add3_u32 v5, v194, v193, s99
	ds_read_b64_tr_b16 v[234:235], v5 offset:16384
	ds_read_b64_tr_b16 v[236:237], v5 offset:16896
	ds_read_b64_tr_b16 v[240:241], v5 offset:16960
	ds_read_b64_tr_b16 v[238:239], v5 offset:16448
	ds_read_b64_tr_b16 v[242:243], v5 offset:18432
	ds_read_b64_tr_b16 v[244:245], v5 offset:18944
	ds_read_b64_tr_b16 v[248:249], v5 offset:19008
	ds_read_b64_tr_b16 v[246:247], v5 offset:18496
	s_waitcnt lgkmcnt(8)
	v_mfma_f32_32x32x16_bf16 v[38:53], v[130:133], v[74:77], v[38:53]
	v_mfma_f32_32x32x16_bf16 v[38:53], v[186:189], v[78:81], v[38:53]
	v_mfma_f32_32x32x16_bf16 v[38:53], v[226:229], v[82:85], v[38:53]
	v_mfma_f32_32x32x16_bf16 v[38:53], v[230:233], v[86:89], v[38:53]
	s_waitcnt lgkmcnt(0)
	s_cmp_ge_u32 s0, s35
	s_cbranch_scc1 .Lmx2_last
	s_add_i32 s0, s0, 1
	s_cmp_lt_u32 s0, s35
	s_cbranch_scc0 .Lmx2_skip
	s_add_i32 m0, s98, 0x1000
	s_nop 0
	global_load_lds_dwordx4 v[106:107], off
	s_add_i32 m0, s98, 0x0
	v_lshl_add_u64 v[106:107], v[106:107], 0, s[100:101]
	global_load_lds_dwordx4 v[108:109], off
	s_add_i32 m0, s98, 0x1400
	v_lshl_add_u64 v[108:109], v[108:109], 0, s[100:101]
	global_load_lds_dwordx4 v[110:111], off
	s_add_i32 m0, s98, 0x400
	v_lshl_add_u64 v[110:111], v[110:111], 0, s[100:101]
	global_load_lds_dwordx4 v[112:113], off
	s_add_i32 m0, s98, 0x1800
	v_lshl_add_u64 v[112:113], v[112:113], 0, s[100:101]
	global_load_lds_dwordx4 v[114:115], off
	s_add_i32 m0, s98, 0x800
	v_lshl_add_u64 v[114:115], v[114:115], 0, s[100:101]
	global_load_lds_dwordx4 v[116:117], off
	s_add_i32 m0, s98, 0x1c00
	v_lshl_add_u64 v[116:117], v[116:117], 0, s[100:101]
	global_load_lds_dwordx4 v[118:119], off
	s_add_i32 m0, s98, 0xc00
	v_lshl_add_u64 v[118:119], v[118:119], 0, s[100:101]
	global_load_lds_dwordx4 v[120:121], off
	v_lshl_add_u64 v[120:121], v[120:121], 0, s[100:101]

; #define LAS __attribute__((address_space(3)))
; #define BA_TR(off_) __builtin_bit_cast(s16x4, __builtin_amdgcn_ds_read_tr16_b64_v4i16((LAS v4i16_t*)(trb + (off_))))
; #define BA_TR(off_) __builtin_bit_cast(s16x4, __builtin_amdgcn_ds_read_tr16_b64_v4i16((LAS v4i16_t*)(trb + (off_))))
; #define BA_TR(off_) __builtin_bit_cast(s16x4, __builtin_amdgcn_ds_read_tr16_b64_v4i16((LAS v4i16_t*)(trb + (off_))))
; #define BA_TR(off_) __builtin_bit_cast(s16x4, __builtin_amdgcn_ds_read_tr16_b64_v4i16((LAS v4i16_t*)(trb + (off_))))
; __device__ __forceinline__ void band_branch_fast(f32x16& o0, f32x16& o1, f32x4& lsum, unsigned& orw, const bf16x8 (&qf)[4], ...
;     ...
;         const LAS float* tp = tab + (kb_first + 32 * kt + tboff);
;         f32x16 s;
; #pragma unroll
;         for (int r = 0; r < 16; ++r) s[r] = tp[(r & 7) + 16 * (r >> 3)];
;         s16x4 vt[8];
; #pragma unroll
;         for (int i = 0; i < 8; ++i) vt[i] = BA_TR((i >> 2) * 2048 + ((i >> 1) & 1) * 64 + (i & 1) * 512);
;         __builtin_amdgcn_sched_barrier(0);
; #pragma unroll
;         for (int d0 = 0; d0 < 4; ++d0) s = __builtin_amdgcn_mfma_f32_32x32x16_bf16(kf[d0], qf[d0], s, 0, 0, 0);
; __device__ __forceinline__ void mixer_a_phase(const bf16* AQ, const bf16* AK, const bf16* AV  , bf16* O, float* ST, float* ML, const float* rel_bias, LAS unsigned char* lds, int G, int blk, int tid, int lane, int wave) {
;     ...
;                 band_branch_fast(o0, o1, lsum, orw, qf, Kb, 512, Vb, 512, 4, r & 3, 2048, 128 * a - 64, 8, tab + TA_LEN, -(128 * a + 4 * i5 + (r >> 2)) + 64 + TA_OFF + 8 * hh, vst, lane);
.LBB0_396:
	v_mov_b32_e32 v2, v225
	v_and_b32_e32 v5, 4, v2
	v_mul_u32_u24_e32 v5, 0x909f, v5
	v_add_u32_e32 v2, v2, v5
	s_mov_b32 s0, s36
	s_branch .LBB0_398
.LBB0_397:
	v_add3_u32 v38, v195, v200, s99
	v_add3_u32 v39, v195, v201, s99
	ds_read_b128 v[186:189], v38 offset:20480
	ds_read_b128 v[226:229], v39 offset:20480
	v_add3_u32 v38, v195, v202, s99
	v_add3_u32 v39, v195, v203, s99
	ds_read_b128 v[230:233], v38 offset:20480
	ds_read_b128 v[234:237], v39 offset:20480
	ds_read_b64 v[38:39], v2
	ds_read_b64 v[40:41], v2 offset:8
	ds_read_b64 v[42:43], v2 offset:16
	ds_read_b64 v[44:45], v2 offset:24
	ds_read_b64 v[46:47], v2 offset:64
	ds_read_b64 v[48:49], v2 offset:72
	ds_read_b64 v[50:51], v2 offset:80
	ds_read_b64 v[52:53], v2 offset:88
	v_add3_u32 v137, v194, v193, s99
	ds_read_b64_tr_b16 v[238:239], v137 offset:16384
	ds_read_b64_tr_b16 v[240:241], v137 offset:16896
	ds_read_b64_tr_b16 v[244:245], v137 offset:16960
	ds_read_b64_tr_b16 v[242:243], v137 offset:16448
	ds_read_b64_tr_b16 v[246:247], v137 offset:18432
	ds_read_b64_tr_b16 v[248:249], v137 offset:18944
	ds_read_b64_tr_b16 v[252:253], v137 offset:19008
	ds_read_b64_tr_b16 v[250:251], v137 offset:18496
	s_waitcnt lgkmcnt(8)
	v_mfma_f32_32x32x16_bf16 v[38:53], v[186:189], v[74:77], v[38:53]
	v_mfma_f32_32x32x16_bf16 v[38:53], v[226:229], v[78:81], v[38:53]
	v_mfma_f32_32x32x16_bf16 v[38:53], v[230:233], v[82:85], v[38:53]
	v_mfma_f32_32x32x16_bf16 v[38:53], v[234:237], v[86:89], v[38:53]
	s_waitcnt lgkmcnt(0)
	s_add_i32 s0, s0, 1
	s_cmp_lt_u32 s0, s37
	s_cbranch_scc0 .Lmx3_skip
	s_add_i32 m0, s98, 0x1000
	s_nop 0
	global_load_lds_dwordx4 v[106:107], off
	s_add_i32 m0, s98, 0x0
	v_lshl_add_u64 v[106:107], v[106:107], 0, s[20:21]
	global_load_lds_dwordx4 v[108:109], off
	s_add_i32 m0, s98, 0x1400
	v_lshl_add_u64 v[108:109], v[108:109], 0, s[20:21]
	global_load_lds_dwordx4 v[110:111], off
	s_add_i32 m0, s98, 0x400
	v_lshl_add_u64 v[110:111], v[110:111], 0, s[20:21]
	global_load_lds_dwordx4 v[112:113], off
	s_add_i32 m0, s98, 0x1800
	v_lshl_add_u64 v[112:113], v[112:113], 0, s[20:21]
	global_load_lds_dwordx4 v[114:115], off
	s_add_i32 m0, s98, 0x800
	v_lshl_add_u64 v[114:115], v[114:115], 0, s[20:21]
	global_load_lds_dwordx4 v[116:117], off
	s_add_i32 m0, s98, 0x1c00
	v_lshl_add_u64 v[116:117], v[116:117], 0, s[20:21]
	global_load_lds_dwordx4 v[118:119], off
	s_add_i32 m0, s98, 0xc00
	v_lshl_add_u64 v[118:119], v[118:119], 0, s[20:21]
	global_load_lds_dwordx4 v[120:121], off
	v_lshl_add_u64 v[120:121], v[120:121], 0, s[20:21]

; #define LAS __attribute__((address_space(3)))
; __global__ void __launch_bounds__(NWAVES * 64, 2) enc_fwd(Args args) {
;     extern __shared__ __attribute__((aligned(16))) unsigned char lds_raw[];
;     LAS unsigned char* lds = (LAS unsigned char*)lds_raw;
	.amdhsa_kernel _Z7enc_fwd4Args
		.amdhsa_group_segment_fixed_size 15872
		.amdhsa_private_segment_fixed_size 0
		.amdhsa_kernarg_size 480
		.amdhsa_user_sgpr_count 2
		.amdhsa_user_sgpr_dispatch_ptr 0
		.amdhsa_user_sgpr_queue_ptr 0
		.amdhsa_user_sgpr_kernarg_segment_ptr 1
		.amdhsa_user_sgpr_dispatch_id 0
		.amdhsa_user_sgpr_kernarg_preload_length 0
		.amdhsa_user_sgpr_kernarg_preload_offset 0
		.amdhsa_user_sgpr_private_segment_size 0
		.amdhsa_uses_dynamic_stack 0
		.amdhsa_enable_private_segment 0
		.amdhsa_system_sgpr_workgroup_id_x 1
		.amdhsa_system_sgpr_workgroup_id_y 0
		.amdhsa_system_sgpr_workgroup_id_z 0
		.amdhsa_system_sgpr_workgroup_info 0
		.amdhsa_system_vgpr_workitem_id 0
		.amdhsa_next_free_vgpr 256
		.amdhsa_next_free_sgpr 102
		.amdhsa_accum_offset 256
		.amdhsa_reserve_vcc 1
		.amdhsa_float_round_mode_32 0
		.amdhsa_float_round_mode_16_64 0
		.amdhsa_float_denorm_mode_32 3
		.amdhsa_float_denorm_mode_16_64 3
		.amdhsa_dx10_clamp 1
		.amdhsa_ieee_mode 1
		.amdhsa_fp16_overflow 0
		.amdhsa_tg_split 0
		.amdhsa_exception_fp_ieee_invalid_op 0
		.amdhsa_exception_fp_denorm_src 0
		.amdhsa_exception_fp_ieee_div_zero 0
		.amdhsa_exception_fp_ieee_overflow 0
		.amdhsa_exception_fp_ieee_underflow 0
		.amdhsa_exception_fp_ieee_inexact 0
		.amdhsa_exception_int_div_zero 0
	.end_amdhsa_kernel

; __global__ void __launch_bounds__(NWAVES * 64, 2) enc_fwd(Args args) {
;     extern __shared__ __attribute__((aligned(16))) unsigned char lds_raw[];
amdhsa.kernels:
  - .agpr_count:     0
    .args:
      - .offset:         0
        .size:           224
        .value_kind:     by_value
      - .offset:         224
        .size:           4
        .value_kind:     hidden_block_count_x
      - .offset:         228
        .size:           4
        .value_kind:     hidden_block_count_y
      - .offset:         232
        .size:           4
        .value_kind:     hidden_block_count_z
      - .offset:         236
        .size:           2
        .value_kind:     hidden_group_size_x
      - .offset:         238
        .size:           2
        .value_kind:     hidden_group_size_y
      - .offset:         240
        .size:           2
        .value_kind:     hidden_group_size_z
      - .offset:         242
        .size:           2
        .value_kind:     hidden_remainder_x
      - .offset:         244
        .size:           2
        .value_kind:     hidden_remainder_y
      - .offset:         246
        .size:           2
        .value_kind:     hidden_remainder_z
      - .offset:         264
        .size:           8
        .value_kind:     hidden_global_offset_x
      - .offset:         272
        .size:           8
        .value_kind:     hidden_global_offset_y
      - .offset:         280
        .size:           8
        .value_kind:     hidden_global_offset_z
      - .offset:         288
        .size:           2
        .value_kind:     hidden_grid_dims
      - .offset:         344
        .size:           4
        .value_kind:     hidden_dynamic_lds_size
    .group_segment_fixed_size: 15872
    .kernarg_segment_align: 8
    .kernarg_segment_size: 480
    .language:       OpenCL C
    .language_version:
      - 2
      - 0
    .max_flat_workgroup_size: 512
    .name:           _Z7enc_fwd4Args
    .private_segment_fixed_size: 0
    .sgpr_count:     108
    .sgpr_spill_count: 136
    .symbol:         _Z7enc_fwd4Args.kd
    .uniform_work_group_size: 1
    .uses_dynamic_stack: false
    .vgpr_count:     256
    .vgpr_spill_count: 0
    .wavefront_size: 64
